# branch-GEMM epilogue: two vmcnt(0) relaxed to counted waits (they only guard older gate loads, not the younger stores)
# baseline (speedup 1.0000x reference)
.LBB0_895:
	v_add_u32_e32 v166, s83, v182
	v_ashrrev_i32_e32 v167, 31, v166
	v_add_u32_e32 v2, s84, v184
	v_lshlrev_b64 v[4:5], 11, v[166:167]
	s_nop 15
	s_nop 15
	v_lshl_add_u64 v[4:5], s[92:93], 0, v[4:5]
	v_ashrrev_i32_e32 v3, 31, v2
	v_lshl_add_u64 v[4:5], v[4:5], 0, v[2:3]
	global_load_dwordx2 v[168:169], v[4:5], off offset:1024 nt
	global_load_dwordx2 v[164:165], v[4:5], off offset:1152 nt
	v_add_co_u32_e32 v6, vcc, s74, v4
	v_lshlrev_b64 v[166:167], 10, v[166:167]
	s_nop 0
	v_addc_co_u32_e32 v7, vcc, 0, v5, vcc
	global_load_dwordx2 v[162:163], v[6:7], off offset:1024 nt
	global_load_dwordx2 v[160:161], v[6:7], off offset:1152 nt
	v_add_co_u32_e32 v6, vcc, s61, v4
	s_mov_b64 s[0:1], 0x4000
	s_nop 0
	v_addc_co_u32_e32 v7, vcc, 0, v5, vcc
	global_load_dwordx2 v[158:159], v[6:7], off offset:1024 nt
	global_load_dwordx2 v[156:157], v[6:7], off offset:1152 nt
	v_add_co_u32_e32 v6, vcc, s73, v4
	s_waitcnt vmcnt(0)
	v_cvt_pk_f32_fp8_e32 v[170:171], v168
	v_cvt_pk_f32_fp8_sdwa v[172:173], v168 src0_sel:WORD_1
	v_cvt_pk_f32_fp8_e32 v[174:175], v169
	v_cvt_pk_f32_fp8_sdwa v[168:169], v169 src0_sel:WORD_1
	v_mul_f32_e32 v11, 0xbfb8aa3b, v170
	v_min_f32_e32 v11, 0x42700000, v11
	v_exp_f32_e32 v11, v11
	v_mul_f32_e32 v170, 0xbfb8aa3b, v171
	v_min_f32_e32 v170, 0x42700000, v170
	v_exp_f32_e32 v170, v170
	v_add_f32_e32 v11, 1.0, v11
	v_rcp_f32_e32 v11, v11
	v_mul_f32_e32 v171, 0xbfb8aa3b, v172
	v_min_f32_e32 v171, 0x42700000, v171
	v_exp_f32_e32 v171, v171
	v_mul_f32_e32 v11, v136, v11
	v_add_f32_e32 v136, 1.0, v170
	v_rcp_f32_e32 v136, v136
	v_mul_f32_e32 v172, 0xbfb8aa3b, v173
	v_min_f32_e32 v172, 0x42700000, v172
	v_exp_f32_e32 v172, v172
	v_mul_f32_e32 v136, v137, v136
	v_add_f32_e32 v137, 1.0, v171
	v_rcp_f32_e32 v137, v137
	v_mul_f32_e32 v173, 0xbfb8aa3b, v174
	v_min_f32_e32 v173, 0x42700000, v173
	v_exp_f32_e32 v173, v173
	v_mul_f32_e32 v137, v138, v137
	v_add_f32_e32 v138, 1.0, v172
	v_rcp_f32_e32 v138, v138
	v_mul_f32_e32 v174, 0xbfb8aa3b, v175
	v_min_f32_e32 v174, 0x42700000, v174
	v_exp_f32_e32 v174, v174
	v_mul_f32_e32 v138, v139, v138
	v_add_f32_e32 v139, 1.0, v173
	v_rcp_f32_e32 v139, v139
	v_mul_f32_e32 v168, 0xbfb8aa3b, v168
	v_min_f32_e32 v168, 0x42700000, v168
	v_exp_f32_e32 v168, v168
	v_mul_f32_e32 v139, v132, v139
	v_add_f32_e32 v132, 1.0, v174
	v_rcp_f32_e32 v132, v132
	v_mul_f32_e32 v169, 0xbfb8aa3b, v169
	v_min_f32_e32 v169, 0x42700000, v169
	v_exp_f32_e32 v169, v169
	v_mul_f32_e32 v170, v133, v132
	v_add_f32_e32 v132, 1.0, v168
	v_rcp_f32_e32 v132, v132
	v_mov_b32_e32 v133, 0
	v_cvt_pk_fp8_f32 v133, v139, v170
	v_addc_co_u32_e32 v7, vcc, 0, v5, vcc
	v_mul_f32_e32 v134, v134, v132
	v_add_f32_e32 v132, 1.0, v169
	v_rcp_f32_e32 v132, v132
	global_load_dwordx2 v[8:9], v[6:7], off offset:1024 nt
	s_nop 0
	global_load_dwordx2 v[6:7], v[6:7], off offset:1152 nt
	v_mul_f32_e32 v135, v135, v132
	v_mov_b32_e32 v132, 0
	v_cvt_pk_fp8_f32 v132, v11, v136
	v_cvt_pk_fp8_f32 v133, v134, v135 op_sel:[0,0,1]
	v_lshl_add_u64 v[134:135], s[24:25], 0, v[166:167]
	v_lshl_add_u64 v[2:3], v[134:135], 0, v[2:3]
	v_cvt_pk_fp8_f32 v132, v137, v138 op_sel:[0,0,1]
	v_cvt_pk_f32_fp8_e32 v[136:137], v164
	v_cvt_pk_f32_fp8_sdwa v[138:139], v164 src0_sel:WORD_1
	v_cvt_pk_f32_fp8_e32 v[134:135], v165
	global_store_dwordx2 v[2:3], v[132:133], off
	v_mul_f32_e32 v11, 0xbfb8aa3b, v136
	v_min_f32_e32 v11, 0x42700000, v11
	v_exp_f32_e32 v11, v11
	v_mul_f32_e32 v136, 0xbfb8aa3b, v137
	v_min_f32_e32 v136, 0x42700000, v136
	v_exp_f32_e32 v136, v136
	v_add_f32_e32 v11, 1.0, v11
	v_rcp_f32_e32 v11, v11
	v_mul_f32_e32 v137, 0xbfb8aa3b, v138
	v_min_f32_e32 v137, 0x42700000, v137
	v_exp_f32_e32 v137, v137
	v_mul_f32_e32 v11, v128, v11
	v_add_f32_e32 v128, 1.0, v136
	v_rcp_f32_e32 v128, v128
	v_mul_f32_e32 v138, 0xbfb8aa3b, v139
	v_min_f32_e32 v138, 0x42700000, v138
	v_exp_f32_e32 v138, v138
	v_mul_f32_e32 v128, v129, v128
	v_add_f32_e32 v129, 1.0, v137
	v_rcp_f32_e32 v129, v129
	v_mul_f32_e32 v134, 0xbfb8aa3b, v134
	v_min_f32_e32 v134, 0x42700000, v134
	v_exp_f32_e32 v134, v134
	v_mul_f32_e32 v129, v130, v129
	v_add_f32_e32 v130, 1.0, v138
	v_rcp_f32_e32 v130, v130
	v_mul_f32_e32 v135, 0xbfb8aa3b, v135
	v_cvt_pk_f32_fp8_sdwa v[132:133], v165 src0_sel:WORD_1
	v_min_f32_e32 v135, 0x42700000, v135
	v_mul_f32_e32 v130, v131, v130
	v_add_f32_e32 v131, 1.0, v134
	v_exp_f32_e32 v135, v135
	v_rcp_f32_e32 v131, v131
	v_mul_f32_e32 v132, 0xbfb8aa3b, v132
	v_min_f32_e32 v132, 0x42700000, v132
	v_exp_f32_e32 v132, v132
	v_mul_f32_e32 v131, v124, v131
	v_add_f32_e32 v124, 1.0, v135
	v_rcp_f32_e32 v124, v124
	v_mul_f32_e32 v133, 0xbfb8aa3b, v133
	v_min_f32_e32 v133, 0x42700000, v133
	v_exp_f32_e32 v133, v133
	v_mul_f32_e32 v134, v125, v124
	v_add_f32_e32 v124, 1.0, v132
	v_rcp_f32_e32 v124, v124
	v_mov_b32_e32 v125, 0
	v_cvt_pk_fp8_f32 v125, v131, v134
	v_mul_f32_e32 v126, v126, v124
	v_add_f32_e32 v124, 1.0, v133
	v_rcp_f32_e32 v124, v124
	s_nop 0
	v_mul_f32_e32 v127, v127, v124
	v_mov_b32_e32 v124, 0
	v_cvt_pk_fp8_f32 v124, v11, v128
	v_cvt_pk_fp8_f32 v125, v126, v127 op_sel:[0,0,1]
	v_cvt_pk_f32_fp8_sdwa v[126:127], v162 src0_sel:WORD_1
	v_cvt_pk_fp8_f32 v124, v129, v130 op_sel:[0,0,1]
	v_cvt_pk_f32_fp8_e32 v[128:129], v163
	v_cvt_pk_f32_fp8_sdwa v[130:131], v163 src0_sel:WORD_1
	global_store_dwordx2 v[2:3], v[124:125], off offset:128
	v_cvt_pk_f32_fp8_e32 v[124:125], v162
	v_mul_f32_e32 v11, 0xbfb8aa3b, v124
	v_min_f32_e32 v11, 0x42700000, v11
	v_exp_f32_e32 v11, v11
	v_mul_f32_e32 v124, 0xbfb8aa3b, v125
	v_min_f32_e32 v124, 0x42700000, v124
	v_exp_f32_e32 v124, v124
	v_add_f32_e32 v11, 1.0, v11
	v_rcp_f32_e32 v11, v11
	v_mul_f32_e32 v125, 0xbfb8aa3b, v126
	v_min_f32_e32 v125, 0x42700000, v125
	v_exp_f32_e32 v125, v125
	v_mul_f32_e32 v11, v120, v11
	v_add_f32_e32 v120, 1.0, v124
	v_rcp_f32_e32 v120, v120
	v_mul_f32_e32 v126, 0xbfb8aa3b, v127
	v_min_f32_e32 v126, 0x42700000, v126
	v_exp_f32_e32 v126, v126
	v_mul_f32_e32 v120, v121, v120
	v_add_f32_e32 v121, 1.0, v125
	v_rcp_f32_e32 v121, v121
	v_mul_f32_e32 v127, 0xbfb8aa3b, v128
	v_min_f32_e32 v127, 0x42700000, v127
	v_exp_f32_e32 v127, v127
	v_mul_f32_e32 v121, v122, v121
	v_add_f32_e32 v122, 1.0, v126
	v_rcp_f32_e32 v122, v122
	v_mul_f32_e32 v128, 0xbfb8aa3b, v129
	v_min_f32_e32 v128, 0x42700000, v128
	v_exp_f32_e32 v128, v128
	v_mul_f32_e32 v122, v123, v122
	v_add_f32_e32 v123, 1.0, v127
	v_rcp_f32_e32 v123, v123
	v_mul_f32_e32 v129, 0xbfb8aa3b, v130
	v_min_f32_e32 v129, 0x42700000, v129
	v_exp_f32_e32 v129, v129
	v_mul_f32_e32 v123, v116, v123
	v_add_f32_e32 v116, 1.0, v128
	v_rcp_f32_e32 v116, v116
	v_mul_f32_e32 v130, 0xbfb8aa3b, v131
	v_min_f32_e32 v130, 0x42700000, v130
	v_exp_f32_e32 v130, v130
	v_mul_f32_e32 v124, v117, v116
	v_add_f32_e32 v116, 1.0, v129
	v_rcp_f32_e32 v116, v116
	v_mov_b32_e32 v117, 0
	v_cvt_pk_fp8_f32 v117, v123, v124
	v_cvt_pk_f32_fp8_sdwa v[124:125], v161 src0_sel:WORD_1
	v_mul_f32_e32 v118, v118, v116
	v_add_f32_e32 v116, 1.0, v130
	v_rcp_f32_e32 v116, v116
	s_nop 0
	v_mul_f32_e32 v119, v119, v116
	v_mov_b32_e32 v116, 0
	v_cvt_pk_fp8_f32 v116, v11, v120
	v_cvt_pk_fp8_f32 v117, v118, v119 op_sel:[0,0,1]
	v_lshl_add_u64 v[118:119], v[2:3], 0, s[0:1]
	s_movk_i32 s0, 0x4000
	v_cvt_pk_fp8_f32 v116, v121, v122 op_sel:[0,0,1]
	v_add_co_u32_e32 v120, vcc, s0, v2
	v_cvt_pk_f32_fp8_e32 v[122:123], v161
	s_nop 0
	v_addc_co_u32_e32 v121, vcc, 0, v3, vcc
	global_store_dwordx2 v[120:121], v[116:117], off
	v_cvt_pk_f32_fp8_e32 v[116:117], v160
	v_cvt_pk_f32_fp8_sdwa v[120:121], v160 src0_sel:WORD_1
	s_mov_b64 s[0:1], 0x8000
	v_mul_f32_e32 v11, 0xbfb8aa3b, v116
	v_min_f32_e32 v11, 0x42700000, v11
	v_exp_f32_e32 v11, v11
	v_mul_f32_e32 v116, 0xbfb8aa3b, v117
	v_min_f32_e32 v116, 0x42700000, v116
	v_exp_f32_e32 v116, v116
	v_add_f32_e32 v11, 1.0, v11
	v_rcp_f32_e32 v11, v11
	v_mul_f32_e32 v117, 0xbfb8aa3b, v120
	v_min_f32_e32 v117, 0x42700000, v117
	v_exp_f32_e32 v117, v117
	v_mul_f32_e32 v11, v112, v11
	v_add_f32_e32 v112, 1.0, v116
	v_rcp_f32_e32 v112, v112
	v_mul_f32_e32 v120, 0xbfb8aa3b, v121
	v_min_f32_e32 v120, 0x42700000, v120
	v_exp_f32_e32 v120, v120
	v_mul_f32_e32 v112, v113, v112
	v_add_f32_e32 v113, 1.0, v117
	v_rcp_f32_e32 v113, v113
	v_mul_f32_e32 v121, 0xbfb8aa3b, v122
	v_min_f32_e32 v121, 0x42700000, v121
	v_exp_f32_e32 v121, v121
	v_mul_f32_e32 v113, v114, v113
	v_add_f32_e32 v114, 1.0, v120
	v_rcp_f32_e32 v114, v114
	v_mul_f32_e32 v122, 0xbfb8aa3b, v123
	v_min_f32_e32 v122, 0x42700000, v122
	v_exp_f32_e32 v122, v122
	v_mul_f32_e32 v114, v115, v114
	v_add_f32_e32 v115, 1.0, v121
	v_rcp_f32_e32 v115, v115
	v_mul_f32_e32 v123, 0xbfb8aa3b, v124
	v_min_f32_e32 v123, 0x42700000, v123
	v_exp_f32_e32 v123, v123
	v_mul_f32_e32 v115, v108, v115
	v_add_f32_e32 v108, 1.0, v122
	v_rcp_f32_e32 v108, v108
	v_mul_f32_e32 v124, 0xbfb8aa3b, v125
	v_min_f32_e32 v124, 0x42700000, v124
	v_exp_f32_e32 v124, v124
	v_mul_f32_e32 v116, v109, v108
	v_add_f32_e32 v108, 1.0, v123
	v_rcp_f32_e32 v108, v108
	v_mov_b32_e32 v109, 0
	v_cvt_pk_fp8_f32 v109, v115, v116
	v_mul_f32_e32 v110, v110, v108
	v_add_f32_e32 v108, 1.0, v124
	v_rcp_f32_e32 v108, v108
	s_nop 0
	v_mul_f32_e32 v111, v111, v108
	v_mov_b32_e32 v108, 0
	v_cvt_pk_fp8_f32 v108, v11, v112
	v_cvt_pk_fp8_f32 v109, v110, v111 op_sel:[0,0,1]
	v_cvt_pk_f32_fp8_sdwa v[110:111], v158 src0_sel:WORD_1
	v_cvt_pk_fp8_f32 v108, v113, v114 op_sel:[0,0,1]
	v_cvt_pk_f32_fp8_e32 v[112:113], v159
	v_cvt_pk_f32_fp8_sdwa v[114:115], v159 src0_sel:WORD_1
	global_store_dwordx2 v[118:119], v[108:109], off offset:128
	v_cvt_pk_f32_fp8_e32 v[108:109], v158
	v_mul_f32_e32 v11, 0xbfb8aa3b, v108
	v_min_f32_e32 v11, 0x42700000, v11
	v_exp_f32_e32 v11, v11
	v_mul_f32_e32 v108, 0xbfb8aa3b, v109
	v_min_f32_e32 v108, 0x42700000, v108
	v_exp_f32_e32 v108, v108
	v_add_f32_e32 v11, 1.0, v11
	v_rcp_f32_e32 v11, v11
	v_mul_f32_e32 v109, 0xbfb8aa3b, v110
	v_min_f32_e32 v109, 0x42700000, v109
	v_exp_f32_e32 v109, v109
	v_mul_f32_e32 v11, v104, v11
	v_add_f32_e32 v104, 1.0, v108
	v_rcp_f32_e32 v104, v104
	v_mul_f32_e32 v110, 0xbfb8aa3b, v111
	v_min_f32_e32 v110, 0x42700000, v110
	v_exp_f32_e32 v110, v110
	v_mul_f32_e32 v104, v105, v104
	v_add_f32_e32 v105, 1.0, v109
	v_rcp_f32_e32 v105, v105
	v_mul_f32_e32 v111, 0xbfb8aa3b, v112
	v_min_f32_e32 v111, 0x42700000, v111
	v_exp_f32_e32 v111, v111
	v_mul_f32_e32 v105, v106, v105
	v_add_f32_e32 v106, 1.0, v110
	v_rcp_f32_e32 v106, v106
	v_mul_f32_e32 v112, 0xbfb8aa3b, v113
	v_min_f32_e32 v112, 0x42700000, v112
	v_exp_f32_e32 v112, v112
	v_mul_f32_e32 v106, v107, v106
	v_add_f32_e32 v107, 1.0, v111
	v_rcp_f32_e32 v107, v107
	v_mul_f32_e32 v113, 0xbfb8aa3b, v114
	v_min_f32_e32 v113, 0x42700000, v113
	v_exp_f32_e32 v113, v113
	v_mul_f32_e32 v107, v100, v107
	v_add_f32_e32 v100, 1.0, v112
	v_rcp_f32_e32 v100, v100
	v_mul_f32_e32 v114, 0xbfb8aa3b, v115
	v_min_f32_e32 v114, 0x42700000, v114
	v_exp_f32_e32 v114, v114
	v_mul_f32_e32 v108, v101, v100
	v_add_f32_e32 v100, 1.0, v113
	v_rcp_f32_e32 v100, v100
	v_mov_b32_e32 v101, 0
	v_cvt_pk_fp8_f32 v101, v107, v108
	v_cvt_pk_f32_fp8_sdwa v[108:109], v157 src0_sel:WORD_1
	v_mul_f32_e32 v102, v102, v100
	v_add_f32_e32 v100, 1.0, v114
	v_rcp_f32_e32 v100, v100
	s_nop 0
	v_mul_f32_e32 v103, v103, v100
	v_mov_b32_e32 v100, 0
	v_cvt_pk_fp8_f32 v100, v11, v104
	v_cvt_pk_fp8_f32 v101, v102, v103 op_sel:[0,0,1]
	v_add_co_u32_e32 v104, vcc, s74, v2
	v_cvt_pk_fp8_f32 v100, v105, v106 op_sel:[0,0,1]
	s_nop 0
	v_addc_co_u32_e32 v105, vcc, 0, v3, vcc
	v_cvt_pk_f32_fp8_e32 v[106:107], v157
	global_store_dwordx2 v[104:105], v[100:101], off
	v_cvt_pk_f32_fp8_e32 v[100:101], v156
	v_cvt_pk_f32_fp8_sdwa v[104:105], v156 src0_sel:WORD_1
	v_lshl_add_u64 v[102:103], v[2:3], 0, s[0:1]
	s_mov_b64 s[0:1], 0xc000
	v_mul_f32_e32 v11, 0xbfb8aa3b, v100
	v_min_f32_e32 v11, 0x42700000, v11
	v_exp_f32_e32 v11, v11
	v_mul_f32_e32 v100, 0xbfb8aa3b, v101
	v_min_f32_e32 v100, 0x42700000, v100
	v_exp_f32_e32 v100, v100
	v_add_f32_e32 v11, 1.0, v11
	v_rcp_f32_e32 v11, v11
	v_mul_f32_e32 v101, 0xbfb8aa3b, v104
	v_min_f32_e32 v101, 0x42700000, v101
	v_exp_f32_e32 v101, v101
	v_mul_f32_e32 v11, v96, v11
	v_add_f32_e32 v96, 1.0, v100
	v_rcp_f32_e32 v96, v96
	v_mul_f32_e32 v104, 0xbfb8aa3b, v105
	v_min_f32_e32 v104, 0x42700000, v104
	v_exp_f32_e32 v104, v104
	v_mul_f32_e32 v96, v97, v96
	v_add_f32_e32 v97, 1.0, v101
	v_rcp_f32_e32 v97, v97
	v_mul_f32_e32 v105, 0xbfb8aa3b, v106
	v_min_f32_e32 v105, 0x42700000, v105
	v_exp_f32_e32 v105, v105
	v_mul_f32_e32 v97, v98, v97
	v_add_f32_e32 v98, 1.0, v104
	v_rcp_f32_e32 v98, v98
	v_mul_f32_e32 v106, 0xbfb8aa3b, v107
	v_min_f32_e32 v106, 0x42700000, v106
	v_exp_f32_e32 v106, v106
	v_mul_f32_e32 v98, v99, v98
	v_add_f32_e32 v99, 1.0, v105
	v_rcp_f32_e32 v99, v99
	v_mul_f32_e32 v107, 0xbfb8aa3b, v108
	v_min_f32_e32 v107, 0x42700000, v107
	v_exp_f32_e32 v107, v107
	v_mul_f32_e32 v99, v92, v99
	v_add_f32_e32 v92, 1.0, v106
	v_rcp_f32_e32 v92, v92
	v_mul_f32_e32 v108, 0xbfb8aa3b, v109
	v_min_f32_e32 v108, 0x42700000, v108
	v_exp_f32_e32 v108, v108
	v_mul_f32_e32 v100, v93, v92
	v_add_f32_e32 v92, 1.0, v107
	v_rcp_f32_e32 v92, v92
	v_mov_b32_e32 v93, 0
	v_cvt_pk_fp8_f32 v93, v99, v100
	v_mul_f32_e32 v94, v94, v92
	v_add_f32_e32 v92, 1.0, v108
	v_rcp_f32_e32 v92, v92
	s_nop 0
	v_mul_f32_e32 v95, v95, v92
	v_mov_b32_e32 v92, 0
	v_cvt_pk_fp8_f32 v92, v11, v96
	v_cvt_pk_fp8_f32 v93, v94, v95 op_sel:[0,0,1]
	s_waitcnt vmcnt(5)
	v_cvt_pk_f32_fp8_sdwa v[94:95], v8 src0_sel:WORD_1
	v_cvt_pk_fp8_f32 v92, v97, v98 op_sel:[0,0,1]
	v_cvt_pk_f32_fp8_e32 v[96:97], v9
	global_store_dwordx2 v[102:103], v[92:93], off offset:128
	v_cvt_pk_f32_fp8_e32 v[92:93], v8
	v_cvt_pk_f32_fp8_sdwa v[8:9], v9 src0_sel:WORD_1
	v_mul_f32_e32 v11, 0xbfb8aa3b, v92
	v_min_f32_e32 v11, 0x42700000, v11
	v_exp_f32_e32 v11, v11
	v_mul_f32_e32 v92, 0xbfb8aa3b, v93
	v_min_f32_e32 v92, 0x42700000, v92
	v_exp_f32_e32 v92, v92
	v_add_f32_e32 v11, 1.0, v11
	v_rcp_f32_e32 v11, v11
	v_mul_f32_e32 v93, 0xbfb8aa3b, v94
	v_min_f32_e32 v93, 0x42700000, v93
	v_exp_f32_e32 v93, v93
	v_mul_f32_e32 v11, v88, v11
	v_add_f32_e32 v88, 1.0, v92
	v_rcp_f32_e32 v88, v88
	v_mul_f32_e32 v94, 0xbfb8aa3b, v95
	v_min_f32_e32 v94, 0x42700000, v94
	v_exp_f32_e32 v94, v94
	v_mul_f32_e32 v88, v89, v88
	v_add_f32_e32 v89, 1.0, v93
	v_rcp_f32_e32 v89, v89
	v_mul_f32_e32 v95, 0xbfb8aa3b, v96
	v_mul_f32_e32 v8, 0xbfb8aa3b, v8
	v_min_f32_e32 v95, 0x42700000, v95
	v_min_f32_e32 v8, 0x42700000, v8
	v_mul_f32_e32 v89, v90, v89
	v_add_f32_e32 v90, 1.0, v94
	v_exp_f32_e32 v95, v95
	v_exp_f32_e32 v8, v8
	v_rcp_f32_e32 v90, v90
	v_mul_f32_e32 v96, 0xbfb8aa3b, v97
	v_mul_f32_e32 v9, 0xbfb8aa3b, v9
	v_min_f32_e32 v96, 0x42700000, v96
	v_min_f32_e32 v9, 0x42700000, v9
	v_mul_f32_e32 v90, v91, v90
	v_add_f32_e32 v91, 1.0, v95
	v_add_f32_e32 v8, 1.0, v8
	v_exp_f32_e32 v96, v96
	v_exp_f32_e32 v9, v9
	v_rcp_f32_e32 v91, v91
	v_rcp_f32_e32 v8, v8
	v_mul_f32_e32 v84, v84, v91
	v_add_f32_e32 v91, 1.0, v96
	v_mul_f32_e32 v86, v86, v8
	v_add_f32_e32 v8, 1.0, v9
	v_rcp_f32_e32 v91, v91
	v_rcp_f32_e32 v8, v8
	v_mov_b32_e32 v9, 0
	v_mul_f32_e32 v85, v85, v91
	v_mul_f32_e32 v87, v87, v8
	v_mov_b32_e32 v8, 0
	v_cvt_pk_fp8_f32 v8, v11, v88
	v_cvt_pk_fp8_f32 v9, v84, v85
	v_lshl_add_u64 v[84:85], v[2:3], 0, s[0:1]
	s_mov_b32 s0, 0xc000
	v_cvt_pk_fp8_f32 v8, v89, v90 op_sel:[0,0,1]
	v_cvt_pk_fp8_f32 v9, v86, v87 op_sel:[0,0,1]
	v_add_co_u32_e32 v86, vcc, s0, v2
	v_cvt_pk_f32_fp8_e32 v[88:89], v7
	s_nop 0
	v_addc_co_u32_e32 v87, vcc, 0, v3, vcc
	global_store_dwordx2 v[86:87], v[8:9], off
	v_cvt_pk_f32_fp8_e32 v[8:9], v6
	v_cvt_pk_f32_fp8_sdwa v[86:87], v6 src0_sel:WORD_1
	v_cvt_pk_f32_fp8_sdwa v[6:7], v7 src0_sel:WORD_1
	s_mov_b64 s[0:1], 0x20000
	v_mul_f32_e32 v9, 0xbfb8aa3b, v9
	v_min_f32_e32 v9, 0x42700000, v9
	v_exp_f32_e32 v9, v9
	v_mul_f32_e32 v11, 0xbfb8aa3b, v86
	v_mul_f32_e32 v86, 0xbfb8aa3b, v87
	v_mul_f32_e32 v87, 0xbfb8aa3b, v88
	v_mul_f32_e32 v6, 0xbfb8aa3b, v6
	v_min_f32_e32 v87, 0x42700000, v87
	v_min_f32_e32 v6, 0x42700000, v6
	v_add_f32_e32 v9, 1.0, v9
	v_exp_f32_e32 v87, v87
	v_exp_f32_e32 v6, v6
	v_rcp_f32_e32 v9, v9
	v_mul_f32_e32 v8, 0xbfb8aa3b, v8
	v_min_f32_e32 v8, 0x42700000, v8
	v_mul_f32_e32 v88, 0xbfb8aa3b, v89
	v_mul_f32_e32 v7, 0xbfb8aa3b, v7
	v_exp_f32_e32 v8, v8
	v_min_f32_e32 v88, 0x42700000, v88
	v_min_f32_e32 v7, 0x42700000, v7
	v_mul_f32_e32 v9, v81, v9
	v_add_f32_e32 v81, 1.0, v87
	v_add_f32_e32 v6, 1.0, v6
	v_exp_f32_e32 v88, v88
	v_exp_f32_e32 v7, v7
	v_rcp_f32_e32 v81, v81
	v_rcp_f32_e32 v6, v6
	v_min_f32_e32 v11, 0x42700000, v11
	v_min_f32_e32 v86, 0x42700000, v86
	v_add_f32_e32 v8, 1.0, v8
	v_exp_f32_e32 v11, v11
	v_exp_f32_e32 v86, v86
	v_rcp_f32_e32 v8, v8
	v_mul_f32_e32 v76, v76, v81
	v_add_f32_e32 v81, 1.0, v88
	v_mul_f32_e32 v78, v78, v6
	v_add_f32_e32 v6, 1.0, v7
	v_rcp_f32_e32 v81, v81
	v_rcp_f32_e32 v6, v6
	v_mul_f32_e32 v8, v80, v8
	v_add_f32_e32 v11, 1.0, v11
	v_add_f32_e32 v80, 1.0, v86
	v_rcp_f32_e32 v11, v11
	v_rcp_f32_e32 v80, v80
	v_mul_f32_e32 v77, v77, v81
	v_mul_f32_e32 v79, v79, v6
	v_mov_b32_e32 v6, 0
	v_mov_b32_e32 v7, 0
	v_cvt_pk_fp8_f32 v6, v8, v9
	v_cvt_pk_fp8_f32 v7, v76, v77
	v_mul_f32_e32 v11, v82, v11
	v_mul_f32_e32 v80, v83, v80
	v_cvt_pk_fp8_f32 v6, v11, v80 op_sel:[0,0,1]
	v_cvt_pk_fp8_f32 v7, v78, v79 op_sel:[0,0,1]
	global_store_dwordx2 v[84:85], v[6:7], off offset:128
	v_add_co_u32_e32 v6, vcc, s76, v4
	s_nop 1
	v_addc_co_u32_e32 v7, vcc, 0, v5, vcc
	global_load_dwordx2 v[82:83], v[6:7], off offset:1024 nt
	global_load_dwordx2 v[84:85], v[6:7], off offset:1152 nt
	v_add_co_u32_e32 v6, vcc, s77, v4
	s_waitcnt vmcnt(0)
	v_cvt_pk_f32_fp8_e32 v[86:87], v82
	v_cvt_pk_f32_fp8_sdwa v[88:89], v82 src0_sel:WORD_1
	v_cvt_pk_f32_fp8_e32 v[90:91], v83
	v_cvt_pk_f32_fp8_sdwa v[82:83], v83 src0_sel:WORD_1
	v_mul_f32_e32 v11, 0xbfb8aa3b, v86
	v_min_f32_e32 v11, 0x42700000, v11
	v_exp_f32_e32 v11, v11
	v_mul_f32_e32 v86, 0xbfb8aa3b, v87
	v_min_f32_e32 v86, 0x42700000, v86
	v_exp_f32_e32 v86, v86
	v_add_f32_e32 v11, 1.0, v11
	v_rcp_f32_e32 v11, v11
	v_mul_f32_e32 v87, 0xbfb8aa3b, v88
	v_min_f32_e32 v87, 0x42700000, v87
	v_exp_f32_e32 v87, v87
	v_mul_f32_e32 v11, v72, v11
	v_add_f32_e32 v72, 1.0, v86
	v_rcp_f32_e32 v72, v72
	v_mul_f32_e32 v88, 0xbfb8aa3b, v89
	v_min_f32_e32 v88, 0x42700000, v88
	v_exp_f32_e32 v88, v88
	v_mul_f32_e32 v72, v73, v72
	v_add_f32_e32 v73, 1.0, v87
	v_rcp_f32_e32 v73, v73
	v_mul_f32_e32 v89, 0xbfb8aa3b, v90
	v_min_f32_e32 v89, 0x42700000, v89
	v_exp_f32_e32 v89, v89
	v_mul_f32_e32 v73, v74, v73
	v_add_f32_e32 v74, 1.0, v88
	v_rcp_f32_e32 v74, v74
	v_mul_f32_e32 v90, 0xbfb8aa3b, v91
	v_min_f32_e32 v90, 0x42700000, v90
	v_exp_f32_e32 v90, v90
	v_mul_f32_e32 v74, v75, v74
	v_add_f32_e32 v75, 1.0, v89
	v_rcp_f32_e32 v75, v75
	v_mul_f32_e32 v82, 0xbfb8aa3b, v82
	v_min_f32_e32 v82, 0x42700000, v82
	v_exp_f32_e32 v82, v82
	v_mul_f32_e32 v75, v68, v75
	v_add_f32_e32 v68, 1.0, v90
	v_rcp_f32_e32 v68, v68
	v_addc_co_u32_e32 v7, vcc, 0, v5, vcc
	global_load_dwordx2 v[80:81], v[6:7], off offset:1024 nt
	global_load_dwordx2 v[78:79], v[6:7], off offset:1152 nt
	v_mul_f32_e32 v83, 0xbfb8aa3b, v83
	v_min_f32_e32 v83, 0x42700000, v83
	v_mul_f32_e32 v86, v69, v68
	v_add_f32_e32 v68, 1.0, v82
	v_exp_f32_e32 v83, v83
	v_rcp_f32_e32 v68, v68
	v_mov_b32_e32 v69, 0
	v_cvt_pk_fp8_f32 v69, v75, v86
	v_add_co_u32_e32 v6, vcc, s78, v4
	v_mul_f32_e32 v70, v70, v68
	v_add_f32_e32 v68, 1.0, v83
	v_rcp_f32_e32 v68, v68
	v_addc_co_u32_e32 v7, vcc, 0, v5, vcc
	v_add_co_u32_e32 v4, vcc, s79, v4
	v_mul_f32_e32 v71, v71, v68
	v_mov_b32_e32 v68, 0
	v_cvt_pk_fp8_f32 v68, v11, v72
	v_cvt_pk_fp8_f32 v69, v70, v71 op_sel:[0,0,1]
	v_addc_co_u32_e32 v5, vcc, 0, v5, vcc
	v_cvt_pk_fp8_f32 v68, v73, v74 op_sel:[0,0,1]
	v_lshl_add_u64 v[70:71], v[2:3], 0, s[0:1]
	s_mov_b32 s0, 0x20000
	v_add_co_u32_e32 v72, vcc, s0, v2
	global_load_dwordx2 v[76:77], v[6:7], off offset:1024 nt
	global_load_dwordx2 v[8:9], v[6:7], off offset:1152 nt
	v_addc_co_u32_e32 v73, vcc, 0, v3, vcc
	global_load_dwordx2 v[6:7], v[4:5], off offset:1024 nt
	s_nop 0
	global_load_dwordx2 v[4:5], v[4:5], off offset:1152 nt
	v_cvt_pk_f32_fp8_e32 v[74:75], v85
	global_store_dwordx2 v[72:73], v[68:69], off
	v_cvt_pk_f32_fp8_e32 v[68:69], v84
	v_cvt_pk_f32_fp8_sdwa v[72:73], v84 src0_sel:WORD_1
	v_cvt_pk_f32_fp8_sdwa v[82:83], v85 src0_sel:WORD_1
	s_mov_b64 s[0:1], 0x24000
	v_mul_f32_e32 v11, 0xbfb8aa3b, v68
	v_min_f32_e32 v11, 0x42700000, v11
	v_exp_f32_e32 v11, v11
	v_mul_f32_e32 v68, 0xbfb8aa3b, v69
	v_min_f32_e32 v68, 0x42700000, v68
	v_exp_f32_e32 v68, v68
	v_add_f32_e32 v11, 1.0, v11
	v_rcp_f32_e32 v11, v11
	v_mul_f32_e32 v69, 0xbfb8aa3b, v72
	v_min_f32_e32 v69, 0x42700000, v69
	v_exp_f32_e32 v69, v69
	v_mul_f32_e32 v11, v64, v11
	v_add_f32_e32 v64, 1.0, v68
	v_rcp_f32_e32 v64, v64
	v_mul_f32_e32 v72, 0xbfb8aa3b, v73
	v_min_f32_e32 v72, 0x42700000, v72
	v_exp_f32_e32 v72, v72
	v_mul_f32_e32 v64, v65, v64
	v_add_f32_e32 v65, 1.0, v69
	v_rcp_f32_e32 v65, v65
	v_mul_f32_e32 v73, 0xbfb8aa3b, v74
	v_min_f32_e32 v73, 0x42700000, v73
	v_exp_f32_e32 v73, v73
	v_mul_f32_e32 v65, v66, v65
	v_add_f32_e32 v66, 1.0, v72
	v_rcp_f32_e32 v66, v66
	v_mul_f32_e32 v74, 0xbfb8aa3b, v75
	v_min_f32_e32 v74, 0x42700000, v74
	v_exp_f32_e32 v74, v74
	v_mul_f32_e32 v66, v67, v66
	v_add_f32_e32 v67, 1.0, v73
	v_rcp_f32_e32 v67, v67
	v_mul_f32_e32 v75, 0xbfb8aa3b, v82
	v_min_f32_e32 v75, 0x42700000, v75
	v_exp_f32_e32 v75, v75
	v_mul_f32_e32 v67, v60, v67
	v_add_f32_e32 v60, 1.0, v74
	v_rcp_f32_e32 v60, v60
	v_mul_f32_e32 v82, 0xbfb8aa3b, v83
	v_min_f32_e32 v82, 0x42700000, v82
	v_exp_f32_e32 v82, v82
	v_mul_f32_e32 v68, v61, v60
	v_add_f32_e32 v60, 1.0, v75
	v_rcp_f32_e32 v60, v60
	v_mov_b32_e32 v61, 0
	v_cvt_pk_fp8_f32 v61, v67, v68
	v_mul_f32_e32 v62, v62, v60
	v_add_f32_e32 v60, 1.0, v82
	v_rcp_f32_e32 v60, v60
	s_nop 0
	v_mul_f32_e32 v63, v63, v60
	v_mov_b32_e32 v60, 0
	v_cvt_pk_fp8_f32 v60, v11, v64
	v_cvt_pk_fp8_f32 v61, v62, v63 op_sel:[0,0,1]
	s_waitcnt vmcnt(1)
	v_cvt_pk_f32_fp8_sdwa v[62:63], v80 src0_sel:WORD_1
	v_cvt_pk_fp8_f32 v60, v65, v66 op_sel:[0,0,1]
	v_cvt_pk_f32_fp8_e32 v[64:65], v81
	v_cvt_pk_f32_fp8_sdwa v[66:67], v81 src0_sel:WORD_1
	global_store_dwordx2 v[70:71], v[60:61], off offset:128
	v_cvt_pk_f32_fp8_e32 v[60:61], v80
	v_mul_f32_e32 v11, 0xbfb8aa3b, v60
	v_min_f32_e32 v11, 0x42700000, v11
	v_exp_f32_e32 v11, v11
	v_mul_f32_e32 v60, 0xbfb8aa3b, v61
	v_min_f32_e32 v60, 0x42700000, v60
	v_exp_f32_e32 v60, v60
	v_add_f32_e32 v11, 1.0, v11
	v_rcp_f32_e32 v11, v11
	v_mul_f32_e32 v61, 0xbfb8aa3b, v62
	v_min_f32_e32 v61, 0x42700000, v61
	v_exp_f32_e32 v61, v61
	v_mul_f32_e32 v11, v56, v11
	v_add_f32_e32 v56, 1.0, v60
	v_rcp_f32_e32 v56, v56
	v_mul_f32_e32 v62, 0xbfb8aa3b, v63
	v_min_f32_e32 v62, 0x42700000, v62
	v_exp_f32_e32 v62, v62
	v_mul_f32_e32 v56, v57, v56
	v_add_f32_e32 v57, 1.0, v61
	v_rcp_f32_e32 v57, v57
	v_mul_f32_e32 v63, 0xbfb8aa3b, v64
	v_min_f32_e32 v63, 0x42700000, v63
	v_exp_f32_e32 v63, v63
	v_mul_f32_e32 v57, v58, v57
	v_add_f32_e32 v58, 1.0, v62
	v_rcp_f32_e32 v58, v58
	v_mul_f32_e32 v64, 0xbfb8aa3b, v65
	v_min_f32_e32 v64, 0x42700000, v64
	v_exp_f32_e32 v64, v64
	v_mul_f32_e32 v58, v59, v58
	v_add_f32_e32 v59, 1.0, v63
	v_rcp_f32_e32 v59, v59
	v_mul_f32_e32 v65, 0xbfb8aa3b, v66
	v_min_f32_e32 v65, 0x42700000, v65
	v_exp_f32_e32 v65, v65
	v_mul_f32_e32 v59, v52, v59
	v_add_f32_e32 v52, 1.0, v64
	v_rcp_f32_e32 v52, v52
	v_mul_f32_e32 v66, 0xbfb8aa3b, v67
	v_min_f32_e32 v66, 0x42700000, v66
	v_exp_f32_e32 v66, v66
	v_mul_f32_e32 v60, v53, v52
	v_add_f32_e32 v52, 1.0, v65
	v_rcp_f32_e32 v52, v52
	v_mov_b32_e32 v53, 0
	v_cvt_pk_fp8_f32 v53, v59, v60
	v_cvt_pk_f32_fp8_sdwa v[60:61], v79 src0_sel:WORD_1
	v_mul_f32_e32 v54, v54, v52
	v_add_f32_e32 v52, 1.0, v66
	v_rcp_f32_e32 v52, v52
	s_nop 0
	v_mul_f32_e32 v55, v55, v52
	v_mov_b32_e32 v52, 0
	v_cvt_pk_fp8_f32 v52, v11, v56
	v_cvt_pk_fp8_f32 v53, v54, v55 op_sel:[0,0,1]
	v_lshl_add_u64 v[54:55], v[2:3], 0, s[0:1]
	s_mov_b32 s0, 0x24000
	v_cvt_pk_fp8_f32 v52, v57, v58 op_sel:[0,0,1]
	v_add_co_u32_e32 v56, vcc, s0, v2
	v_cvt_pk_f32_fp8_e32 v[58:59], v79
	s_nop 0
	v_addc_co_u32_e32 v57, vcc, 0, v3, vcc
	global_store_dwordx2 v[56:57], v[52:53], off
	v_cvt_pk_f32_fp8_e32 v[52:53], v78
	v_cvt_pk_f32_fp8_sdwa v[56:57], v78 src0_sel:WORD_1
	s_mov_b64 s[0:1], 0x28000
	v_mul_f32_e32 v11, 0xbfb8aa3b, v52
	v_min_f32_e32 v11, 0x42700000, v11
	v_exp_f32_e32 v11, v11
	v_mul_f32_e32 v52, 0xbfb8aa3b, v53
	v_min_f32_e32 v52, 0x42700000, v52
	v_exp_f32_e32 v52, v52
	v_add_f32_e32 v11, 1.0, v11
	v_rcp_f32_e32 v11, v11
	v_mul_f32_e32 v53, 0xbfb8aa3b, v56
	v_min_f32_e32 v53, 0x42700000, v53
	v_exp_f32_e32 v53, v53
	v_mul_f32_e32 v11, v48, v11
	v_add_f32_e32 v48, 1.0, v52
	v_rcp_f32_e32 v48, v48
	v_mul_f32_e32 v56, 0xbfb8aa3b, v57
	v_min_f32_e32 v56, 0x42700000, v56
	v_exp_f32_e32 v56, v56
	v_mul_f32_e32 v48, v49, v48
	v_add_f32_e32 v49, 1.0, v53
	v_rcp_f32_e32 v49, v49
	v_mul_f32_e32 v57, 0xbfb8aa3b, v58
	v_min_f32_e32 v57, 0x42700000, v57
	v_exp_f32_e32 v57, v57
	v_mul_f32_e32 v49, v50, v49
	v_add_f32_e32 v50, 1.0, v56
	v_rcp_f32_e32 v50, v50
	v_mul_f32_e32 v58, 0xbfb8aa3b, v59
	v_min_f32_e32 v58, 0x42700000, v58
	v_exp_f32_e32 v58, v58
	v_mul_f32_e32 v50, v51, v50
	v_add_f32_e32 v51, 1.0, v57
	v_rcp_f32_e32 v51, v51
	v_mul_f32_e32 v59, 0xbfb8aa3b, v60
	v_min_f32_e32 v59, 0x42700000, v59
	v_exp_f32_e32 v59, v59
	v_mul_f32_e32 v51, v44, v51
	v_add_f32_e32 v44, 1.0, v58
	v_rcp_f32_e32 v44, v44
	v_mul_f32_e32 v60, 0xbfb8aa3b, v61
	v_min_f32_e32 v60, 0x42700000, v60
	v_exp_f32_e32 v60, v60
	v_mul_f32_e32 v52, v45, v44
	v_add_f32_e32 v44, 1.0, v59
	v_rcp_f32_e32 v44, v44
	v_mov_b32_e32 v45, 0
	v_cvt_pk_fp8_f32 v45, v51, v52
	v_mul_f32_e32 v46, v46, v44
	v_add_f32_e32 v44, 1.0, v60
	v_rcp_f32_e32 v44, v44
	s_nop 0
	v_mul_f32_e32 v47, v47, v44
	v_mov_b32_e32 v44, 0
	v_cvt_pk_fp8_f32 v44, v11, v48
	v_cvt_pk_fp8_f32 v45, v46, v47 op_sel:[0,0,1]
	v_cvt_pk_f32_fp8_sdwa v[46:47], v76 src0_sel:WORD_1
	v_cvt_pk_fp8_f32 v44, v49, v50 op_sel:[0,0,1]
	v_cvt_pk_f32_fp8_e32 v[48:49], v77
	v_cvt_pk_f32_fp8_sdwa v[50:51], v77 src0_sel:WORD_1
	global_store_dwordx2 v[54:55], v[44:45], off offset:128
	v_cvt_pk_f32_fp8_e32 v[44:45], v76
	v_mul_f32_e32 v11, 0xbfb8aa3b, v44
	v_min_f32_e32 v11, 0x42700000, v11
	v_exp_f32_e32 v11, v11
	v_mul_f32_e32 v44, 0xbfb8aa3b, v45
	v_min_f32_e32 v44, 0x42700000, v44
	v_exp_f32_e32 v44, v44
	v_add_f32_e32 v11, 1.0, v11
	v_rcp_f32_e32 v11, v11
	v_mul_f32_e32 v45, 0xbfb8aa3b, v46
	v_min_f32_e32 v45, 0x42700000, v45
	v_exp_f32_e32 v45, v45
	v_mul_f32_e32 v11, v40, v11
	v_add_f32_e32 v40, 1.0, v44
	v_rcp_f32_e32 v40, v40
	v_mul_f32_e32 v46, 0xbfb8aa3b, v47
	v_min_f32_e32 v46, 0x42700000, v46
	v_exp_f32_e32 v46, v46
	v_mul_f32_e32 v40, v41, v40
	v_add_f32_e32 v41, 1.0, v45
	v_rcp_f32_e32 v41, v41
	v_mul_f32_e32 v47, 0xbfb8aa3b, v48
	v_min_f32_e32 v47, 0x42700000, v47
	v_exp_f32_e32 v47, v47
	v_mul_f32_e32 v41, v42, v41
	v_add_f32_e32 v42, 1.0, v46
	v_rcp_f32_e32 v42, v42
	v_mul_f32_e32 v48, 0xbfb8aa3b, v49
	v_min_f32_e32 v48, 0x42700000, v48
	v_exp_f32_e32 v48, v48
	v_mul_f32_e32 v42, v43, v42
	v_add_f32_e32 v43, 1.0, v47
	v_rcp_f32_e32 v43, v43
	v_mul_f32_e32 v49, 0xbfb8aa3b, v50
	v_min_f32_e32 v49, 0x42700000, v49
	v_exp_f32_e32 v49, v49
	v_mul_f32_e32 v43, v36, v43
	v_add_f32_e32 v36, 1.0, v48
	v_rcp_f32_e32 v36, v36
	v_mul_f32_e32 v50, 0xbfb8aa3b, v51
	v_min_f32_e32 v50, 0x42700000, v50
	v_exp_f32_e32 v50, v50
	v_mul_f32_e32 v44, v37, v36
	v_add_f32_e32 v36, 1.0, v49
	v_rcp_f32_e32 v36, v36
	v_mov_b32_e32 v37, 0
	v_cvt_pk_fp8_f32 v37, v43, v44
	v_mul_f32_e32 v38, v38, v36
	v_add_f32_e32 v36, 1.0, v50
	v_rcp_f32_e32 v36, v36
	s_nop 0
	v_mul_f32_e32 v39, v39, v36
	v_mov_b32_e32 v36, 0
	v_cvt_pk_fp8_f32 v36, v11, v40
	v_cvt_pk_fp8_f32 v37, v38, v39 op_sel:[0,0,1]
	v_lshl_add_u64 v[38:39], v[2:3], 0, s[0:1]
	s_mov_b32 s0, 0x28000
	v_cvt_pk_fp8_f32 v36, v41, v42 op_sel:[0,0,1]
	v_add_co_u32_e32 v40, vcc, s0, v2
	v_cvt_pk_f32_fp8_e32 v[42:43], v9
	s_nop 0
	v_addc_co_u32_e32 v41, vcc, 0, v3, vcc
	global_store_dwordx2 v[40:41], v[36:37], off
	v_cvt_pk_f32_fp8_e32 v[36:37], v8
	v_cvt_pk_f32_fp8_sdwa v[40:41], v8 src0_sel:WORD_1
	v_cvt_pk_f32_fp8_sdwa v[8:9], v9 src0_sel:WORD_1
	s_mov_b64 s[0:1], 0x2c000
	v_mul_f32_e32 v11, 0xbfb8aa3b, v36
	v_min_f32_e32 v11, 0x42700000, v11
	v_exp_f32_e32 v11, v11
	v_mul_f32_e32 v36, 0xbfb8aa3b, v37
	v_min_f32_e32 v36, 0x42700000, v36
	v_exp_f32_e32 v36, v36
	v_add_f32_e32 v11, 1.0, v11
	v_rcp_f32_e32 v11, v11
	v_mul_f32_e32 v37, 0xbfb8aa3b, v40
	v_min_f32_e32 v37, 0x42700000, v37
	v_exp_f32_e32 v37, v37
	v_mul_f32_e32 v11, v32, v11
	v_add_f32_e32 v32, 1.0, v36
	v_rcp_f32_e32 v32, v32
	v_mul_f32_e32 v40, 0xbfb8aa3b, v41
	v_min_f32_e32 v40, 0x42700000, v40
	v_exp_f32_e32 v40, v40
	v_mul_f32_e32 v32, v33, v32
	v_add_f32_e32 v33, 1.0, v37
	v_rcp_f32_e32 v33, v33
	v_mul_f32_e32 v41, 0xbfb8aa3b, v42
	v_mul_f32_e32 v8, 0xbfb8aa3b, v8
	v_min_f32_e32 v41, 0x42700000, v41
	v_min_f32_e32 v8, 0x42700000, v8
	v_mul_f32_e32 v33, v34, v33
	v_add_f32_e32 v34, 1.0, v40
	v_exp_f32_e32 v41, v41
	v_exp_f32_e32 v8, v8
	v_rcp_f32_e32 v34, v34
	v_mul_f32_e32 v42, 0xbfb8aa3b, v43
	v_mul_f32_e32 v9, 0xbfb8aa3b, v9
	v_min_f32_e32 v42, 0x42700000, v42
	v_min_f32_e32 v9, 0x42700000, v9
	v_mul_f32_e32 v34, v35, v34
	v_add_f32_e32 v35, 1.0, v41
	v_add_f32_e32 v8, 1.0, v8
	v_exp_f32_e32 v42, v42
	v_exp_f32_e32 v9, v9
	v_rcp_f32_e32 v35, v35
	v_rcp_f32_e32 v8, v8
	v_mul_f32_e32 v28, v28, v35
	v_add_f32_e32 v35, 1.0, v42
	v_mul_f32_e32 v30, v30, v8
	v_add_f32_e32 v8, 1.0, v9
	v_rcp_f32_e32 v35, v35
	v_rcp_f32_e32 v8, v8
	v_mov_b32_e32 v9, 0
	v_mul_f32_e32 v29, v29, v35
	v_mul_f32_e32 v31, v31, v8
	v_mov_b32_e32 v8, 0
	v_cvt_pk_fp8_f32 v8, v11, v32
	v_cvt_pk_fp8_f32 v9, v28, v29
	v_cvt_pk_f32_fp8_sdwa v[28:29], v6 src0_sel:WORD_1
	v_cvt_pk_fp8_f32 v8, v33, v34 op_sel:[0,0,1]
	v_cvt_pk_fp8_f32 v9, v30, v31 op_sel:[0,0,1]
	v_cvt_pk_f32_fp8_e32 v[30:31], v7
	v_mul_f32_e32 v11, 0xbfb8aa3b, v28
	v_mul_f32_e32 v28, 0xbfb8aa3b, v29
	global_store_dwordx2 v[38:39], v[8:9], off offset:128
	v_cvt_pk_f32_fp8_e32 v[8:9], v6
	v_cvt_pk_f32_fp8_sdwa v[6:7], v7 src0_sel:WORD_1
	v_mul_f32_e32 v29, 0xbfb8aa3b, v30
	v_min_f32_e32 v29, 0x42700000, v29
	v_mul_f32_e32 v9, 0xbfb8aa3b, v9
	v_min_f32_e32 v9, 0x42700000, v9
	v_exp_f32_e32 v9, v9
	v_mul_f32_e32 v6, 0xbfb8aa3b, v6
	v_min_f32_e32 v6, 0x42700000, v6
	v_exp_f32_e32 v29, v29
	v_add_f32_e32 v9, 1.0, v9
	v_exp_f32_e32 v6, v6
	v_rcp_f32_e32 v9, v9
	v_mul_f32_e32 v8, 0xbfb8aa3b, v8
	v_min_f32_e32 v8, 0x42700000, v8
	v_mul_f32_e32 v30, 0xbfb8aa3b, v31
	v_mul_f32_e32 v7, 0xbfb8aa3b, v7
	v_exp_f32_e32 v8, v8
	v_min_f32_e32 v30, 0x42700000, v30
	v_min_f32_e32 v7, 0x42700000, v7
	v_mul_f32_e32 v9, v25, v9
	v_add_f32_e32 v25, 1.0, v29
	v_add_f32_e32 v6, 1.0, v6
	v_exp_f32_e32 v30, v30
	v_exp_f32_e32 v7, v7
	v_rcp_f32_e32 v25, v25
	v_rcp_f32_e32 v6, v6
	v_min_f32_e32 v11, 0x42700000, v11
	v_min_f32_e32 v28, 0x42700000, v28
	v_add_f32_e32 v8, 1.0, v8
	v_exp_f32_e32 v11, v11
	v_exp_f32_e32 v28, v28
	v_rcp_f32_e32 v8, v8
	v_mul_f32_e32 v20, v20, v25
	v_add_f32_e32 v25, 1.0, v30
	v_mul_f32_e32 v22, v22, v6
	v_add_f32_e32 v6, 1.0, v7
	v_rcp_f32_e32 v25, v25
	v_rcp_f32_e32 v6, v6
	v_mul_f32_e32 v8, v24, v8
	v_add_f32_e32 v11, 1.0, v11
	v_add_f32_e32 v24, 1.0, v28
	v_rcp_f32_e32 v11, v11
	v_rcp_f32_e32 v24, v24
	v_mul_f32_e32 v21, v21, v25
	v_mul_f32_e32 v23, v23, v6
	v_mov_b32_e32 v6, 0
	v_mov_b32_e32 v7, 0
	v_cvt_pk_fp8_f32 v6, v8, v9
	v_cvt_pk_fp8_f32 v7, v20, v21
	v_mul_f32_e32 v11, v26, v11
	v_mul_f32_e32 v24, v27, v24
	v_cvt_pk_fp8_f32 v6, v11, v24 op_sel:[0,0,1]
	v_cvt_pk_fp8_f32 v7, v22, v23 op_sel:[0,0,1]
	v_lshl_add_u64 v[8:9], v[2:3], 0, s[0:1]
	s_mov_b32 s0, 0x2c000
	v_add_co_u32_e32 v2, vcc, s0, v2
	v_cvt_pk_f32_fp8_e32 v[20:21], v5
	s_nop 0
	v_addc_co_u32_e32 v3, vcc, 0, v3, vcc
	global_store_dwordx2 v[2:3], v[6:7], off
	v_cvt_pk_f32_fp8_e32 v[2:3], v4
	v_cvt_pk_f32_fp8_sdwa v[6:7], v4 src0_sel:WORD_1
	v_mul_f32_e32 v11, 0xbfb8aa3b, v20
	v_min_f32_e32 v11, 0x42700000, v11
	v_mul_f32_e32 v2, 0xbfb8aa3b, v2
	v_min_f32_e32 v2, 0x42700000, v2
	v_exp_f32_e32 v2, v2
	v_mul_f32_e32 v3, 0xbfb8aa3b, v3
	v_min_f32_e32 v3, 0x42700000, v3
	v_exp_f32_e32 v3, v3
	v_add_f32_e32 v2, 1.0, v2
	v_rcp_f32_e32 v2, v2
	v_mul_f32_e32 v6, 0xbfb8aa3b, v6
	v_min_f32_e32 v6, 0x42700000, v6
	v_exp_f32_e32 v6, v6
	v_mul_f32_e32 v16, v16, v2
	v_add_f32_e32 v2, 1.0, v3
	v_rcp_f32_e32 v2, v2
	v_mul_f32_e32 v7, 0xbfb8aa3b, v7
	v_min_f32_e32 v7, 0x42700000, v7
	v_exp_f32_e32 v7, v7
	v_mul_f32_e32 v3, v17, v2
	v_add_f32_e32 v2, 1.0, v6
	v_rcp_f32_e32 v2, v2
	v_exp_f32_e32 v11, v11
	v_mul_f32_e32 v20, 0xbfb8aa3b, v21
	v_cvt_pk_f32_fp8_sdwa v[4:5], v5 src0_sel:WORD_1
	v_mul_f32_e32 v6, v18, v2
	v_add_f32_e32 v2, 1.0, v7
	v_rcp_f32_e32 v2, v2
	v_min_f32_e32 v20, 0x42700000, v20
	v_exp_f32_e32 v20, v20
	v_mul_f32_e32 v4, 0xbfb8aa3b, v4
	v_mul_f32_e32 v7, v19, v2
	v_add_f32_e32 v2, 1.0, v11
	v_rcp_f32_e32 v2, v2
	v_min_f32_e32 v4, 0x42700000, v4
	v_exp_f32_e32 v4, v4
	v_mul_f32_e32 v5, 0xbfb8aa3b, v5
	v_mul_f32_e32 v11, v12, v2
	v_add_f32_e32 v2, 1.0, v20
	v_rcp_f32_e32 v2, v2
	v_min_f32_e32 v5, 0x42700000, v5
	v_exp_f32_e32 v5, v5
	s_mov_b64 s[0:1], -1
	v_mul_f32_e32 v12, v13, v2
	v_add_f32_e32 v2, 1.0, v4
	v_rcp_f32_e32 v2, v2
	s_and_b64 vcc, exec, s[6:7]
	v_mul_f32_e32 v4, v14, v2
	v_add_f32_e32 v2, 1.0, v5
	v_rcp_f32_e32 v2, v2
	s_nop 0
	v_mul_f32_e32 v5, v15, v2
	v_mov_b32_e32 v2, 0
	v_cvt_pk_fp8_f32 v2, v16, v3
	v_mov_b32_e32 v3, 0
	v_cvt_pk_fp8_f32 v3, v11, v12
	v_cvt_pk_fp8_f32 v2, v6, v7 op_sel:[0,0,1]
	v_cvt_pk_fp8_f32 v3, v4, v5 op_sel:[0,0,1]
	global_store_dwordx2 v[8:9], v[2:3], off offset:128
	s_cbranch_vccnz .LBB0_877
	s_andn2_b64 vcc, exec, s[22:23]
	s_cbranch_vccnz .LBB0_876
	s_barrier
	s_branch .LBB0_876
